# c23: c13 plus grid-barrier change - workgroups that are not their XCD's last arriver wait on the top-level generation word directly instead of the per-XCD forwarded word (one hop less in the release c
# baseline (speedup 1.0000x reference)
.LBB0_150:
	s_or_b64 exec, exec, s[10:11]
	v_cvt_f32_u32_e32 v5, v3
	s_waitcnt vmcnt(0)
	v_readfirstlane_b32 s2, v4
	v_sub_u32_e32 v4, 0, v3
	v_rcp_iflag_f32_e32 v5, v5
	v_add_u32_e32 v6, s2, v2
	v_mul_f32_e32 v5, 0x4f7ffffe, v5
	v_cvt_u32_f32_e32 v5, v5
	v_mul_lo_u32 v2, v4, v5
	v_mul_hi_u32 v2, v5, v2
	v_add_u32_e32 v2, v5, v2
	v_mul_hi_u32 v2, v6, v2
	v_mul_lo_u32 v4, v2, v3
	v_sub_u32_e32 v4, v6, v4
	v_add_u32_e32 v5, 1, v2
	v_cmp_ge_u32_e32 vcc, v4, v3
	s_nop 1
	v_cndmask_b32_e32 v2, v2, v5, vcc
	v_sub_u32_e32 v5, v4, v3
	v_cndmask_b32_e32 v4, v4, v5, vcc
	v_add_u32_e32 v5, 1, v2
	v_cmp_ge_u32_e32 vcc, v4, v3
	v_add_u32_e32 v4, 1, v6
	s_nop 0
	v_cndmask_b32_e32 v2, v2, v5, vcc
	v_mul_lo_u32 v5, v3, v2
	v_add_u32_e32 v3, v5, v3
	v_cmp_ne_u32_e32 vcc, v4, v3
	s_and_saveexec_b64 s[2:3], vcc
	s_xor_b64 s[8:9], exec, s[2:3]
	s_cbranch_execz .LBB0_164
	s_waitcnt lgkmcnt(0)
	v_mov_b32_e32 v1, 0x7000
	global_load_dword v1, v1, s[50:51] offset:1280 sc1
	s_add_u32 s14, s50, 0x7500
	s_addc_u32 s15, s51, 0
	s_waitcnt vmcnt(0)
	v_cmp_eq_u32_e32 vcc, v1, v2
	s_and_saveexec_b64 s[10:11], vcc
	s_cbranch_execz .LBB0_163
	s_add_u32 s12, s50, 0x4200
	s_addc_u32 s13, s51, 0
	s_mov_b32 s2, 1
	s_mov_b64 s[16:17], 0
	v_mov_b32_e32 v1, 0
	s_branch .LBB0_154

.LBB0_1537:
	s_or_b64 exec, exec, s[10:11]
	v_cvt_f32_u32_e32 v4, v2
	s_waitcnt vmcnt(0)
	v_readfirstlane_b32 s2, v3
	v_sub_u32_e32 v3, 0, v2
	v_rcp_iflag_f32_e32 v4, v4
	v_add_u32_e32 v5, s2, v1
	v_mul_f32_e32 v4, 0x4f7ffffe, v4
	v_cvt_u32_f32_e32 v4, v4
	v_mul_lo_u32 v1, v3, v4
	v_mul_hi_u32 v1, v4, v1
	v_add_u32_e32 v1, v4, v1
	v_mul_hi_u32 v1, v5, v1
	v_mul_lo_u32 v3, v1, v2
	v_sub_u32_e32 v3, v5, v3
	v_add_u32_e32 v4, 1, v1
	v_cmp_ge_u32_e32 vcc, v3, v2
	s_nop 1
	v_cndmask_b32_e32 v1, v1, v4, vcc
	v_sub_u32_e32 v4, v3, v2
	v_cndmask_b32_e32 v3, v3, v4, vcc
	v_add_u32_e32 v4, 1, v1
	v_cmp_ge_u32_e32 vcc, v3, v2
	v_add_u32_e32 v3, 1, v5
	s_nop 0
	v_cndmask_b32_e32 v1, v1, v4, vcc
	v_mul_lo_u32 v4, v2, v1
	v_add_u32_e32 v2, v4, v2
	v_cmp_ne_u32_e32 vcc, v3, v2
	s_and_saveexec_b64 s[2:3], vcc
	s_xor_b64 s[8:9], exec, s[2:3]
	s_cbranch_execz .LBB0_1551
	s_waitcnt lgkmcnt(0)
	v_mov_b32_e32 v0, 0x7000
	global_load_dword v0, v0, s[50:51] offset:1280 sc1
	s_add_u32 s14, s50, 0x7500
	s_addc_u32 s15, s51, 0
	s_waitcnt vmcnt(0)
	v_cmp_eq_u32_e32 vcc, v0, v1
	s_and_saveexec_b64 s[10:11], vcc
	s_cbranch_execz .LBB0_1550
	s_add_u32 s12, s50, 0x4200
	s_addc_u32 s13, s51, 0
	s_mov_b32 s2, 1
	s_mov_b64 s[16:17], 0
	v_mov_b32_e32 v0, 0
	s_branch .LBB0_1541
